# final6 + per-wave software pipeline in diff attention: 4-slot ring, QK(t+1) accumulates into a second score buffer with its 8 MFMAs interleaved into the row-max tree and first exp chunk of tile t, cop
# speedup vs baseline: 1.0069x; 1.0049x over previous
; #define LAS __attribute__((address_space(3)))
; #define MFMA32(a, b, c) __builtin_amdgcn_mfma_f32_32x32x16_bf16((a), (b), (c), 0, 0, 0)
; DI int at_v_rd_base(int lane) { return ((lane & 3) << 3) | (((lane >> 2) & 3) << 6) | (((lane >> 4) & 1) << 5) | (((lane >> 5) & 1) << 8); }
;     __device__ __forceinline__ void init(const void* A_, const void* B_, int lda_, int ldb_, int M, unsigned mask_, int G_, int c_) { A = (const char*)A_; B = (const char*)B_; lda = lda_; ldb = ldb_; nM = M / BM; mask = mask_; nN = __builtin_popcount(mask_); nwg = nM * nN; G = G_; c = c_; }
; template <int KS> DI void at_qk(f32x16& p0, f32x16& p1, LAS const unsigned char* Kt, int mapB, const bf16x8 (&qr)[8], float init, int r32, int hi) {
; #pragma unroll
;     for (int i = 0; i < 16; ++i) { p0[i] = init; p1[i] = init; }
;     bf16x8 kb[KS][2];
; #pragma unroll
;     for (int d0 = 0; d0 < KS; ++d0) { const int cb = mapB + (d0 * 16 + hi * 8) * 2;
;         kb[d0][0] = *(const LAS bf16x8*)(Kt + AT_KSWZ(r32, cb)); kb[d0][1] = *(const LAS bf16x8*)(Kt + AT_KSWZ(32 + r32, cb)); }
;     __builtin_amdgcn_sched_barrier(0);
; #pragma unroll
;     for (int d0 = 0; d0 < KS; ++d0) { p0 = MFMA32(kb[d0][0], qr[d0], p0); p1 = MFMA32(kb[d0][1], qr[d0], p1); }
; DI void attn_unit_diff(const Ctx& C, int l, int b, int h, int j) {
;     ...
;     f32x16 o[4], ol = {}; float m_run = 0.f; bool first = true;
; #pragma unroll
;     for (int d0 = 0; d0 < 4; ++d0) o[d0] = f32x16{};
;     const bf16x8 ones = {16256, 16256, 16256, 16256, 16256, 16256, 16256, 16256};
;     asm volatile("s_waitcnt vmcnt(0) lgkmcnt(0)\n\ts_barrier" ::: "memory");
;     const float cfar = tabl[0];
;     const int vrd = at_v_rd_base(lane);
;     for (int sd = 0; sd < nt; ++sd) {
;         const int slot = sd % 3;
;         const bool staged = sd + 2 < nt;
;         if (staged) at_stage1(C.lds, projb, kcolB, vcolB, sd + 2, (sd + 2) % 3, wid, lb0, lb1);
;         if (sd <= cw) {
;             LAS const unsigned char* Kt = C.lds + slot * 32768;
;             const int vb = (int)(size_t)(Kt + 16384) + vrd;
;             const bool nearb = (sd * 64 + 63 - q0w) > -305;
;             LAS const float* tabp = tabl + (sd * 64 - qpos + TABB_OFF + 4 * hi);
;             f32x16 p0, p1;
;             at_qk<KS>(p0, p1, Kt, g * 128, qr, (nearb ? 0.f : cfar) - m_run, r32, hi);
.LBB0_785:
	s_or_b64 exec, exec, s[38:39]
	s_add_i32 s50, 0, 0x20000
	s_lshr_b32 s28, s97, 4
	s_lshl_b32 s66, s49, 1
	v_readlane_b32 s38, v252, 22
	s_waitcnt vmcnt(0) lgkmcnt(0)
	s_barrier
	v_mov_b32_e32 v4, s50
	s_and_b32 s28, s28, 7
	s_or_b32 s67, s66, s38
	s_waitcnt lgkmcnt(0)
	ds_read_b32 v158, v4
	v_and_b32_e32 v4, 24, v8
	v_and_b32_e32 v7, 0x100, v8
	v_lshlrev_b32_e32 v8, 4, v156
	v_readlane_b32 s38, v252, 26
	s_lshl_b32 s28, s28, 8
	v_lshlrev_b32_e32 v145, 4, v154
	v_add_u32_e32 v9, s38, v8
	v_readlane_b32 s38, v252, 23
	v_lshlrev_b32_e32 v11, 4, v155
	v_lshlrev_b32_e32 v15, 2, v154
	s_add_i32 s88, s55, 0xfffffe90
	s_add_i32 s38, s38, s52
	s_add_i32 s91, 0, 0x4000
	s_add_i32 s52, s48, s28
	v_mov_b32_e32 v3, v1
	v_and_b32_e32 v5, 0xc0, v145
	v_lshlrev_b32_e32 v6, 1, v154
	v_lshlrev_b32_e32 v10, 8, v155
	v_and_b32_e32 v11, 0x70, v11
	v_add_u32_e32 v14, 0x60, v9
	v_xor_b32_e32 v157, 0x80, v15
	v_add_lshl_u32 v15, s38, v155, 2
	s_add_u32 s38, s96, s42
	v_and_b32_e32 v6, 32, v6
	v_add_u32_e32 v12, 32, v9
	v_add_u32_e32 v13, 64, v9
	v_sub_u32_e32 v159, v8, v15
	v_add3_u32 v5, v7, s91, v5
	v_xad_u32 v164, v14, v11, v10
	v_lshl_add_u64 v[2:3], s[42:43], 0, v[2:3]
	s_addc_u32 s39, s89, s43
	v_mov_b32_e32 v14, v1
	v_mov_b32_e32 v15, v1
	v_add3_u32 v160, v5, v6, v4
	v_xad_u32 v161, v9, v11, v10
	v_xad_u32 v162, v12, v11, v10
	v_xad_u32 v163, v13, v11, v10
	v_lshl_add_u64 v[146:147], s[70:71], 0, v[2:3]
	v_lshl_add_u64 v[148:149], s[72:73], 0, v[2:3]
	v_lshl_add_u64 v[150:151], s[38:39], 0, v[0:1]
	s_lshl_b32 s95, s49, 16
	v_mov_b32_e32 v0, v1
	v_mov_b32_e32 v2, v1
	v_mov_b32_e32 v3, v1
	v_mov_b32_e32 v4, v1
	v_mov_b32_e32 v5, v1
	v_mov_b32_e32 v6, v1
	v_mov_b32_e32 v7, v1
	v_mov_b32_e32 v8, v1
	v_mov_b32_e32 v9, v1
	v_mov_b32_e32 v10, v1
	v_mov_b32_e32 v11, v1
	v_mov_b32_e32 v12, v1
	v_mov_b32_e32 v13, v1
	v_mov_b64_e32 v[78:79], v[14:15]
	v_mov_b64_e32 v[62:63], v[14:15]
	v_mov_b64_e32 v[46:47], v[14:15]
	v_mov_b64_e32 v[30:31], v[14:15]
	v_mov_b64_e32 v[94:95], v[14:15]
	s_mov_b32 s79, 2
	s_add_i32 s95, s95, 0x10000
	s_mov_b32 s48, 0
	v_mov_b32_e32 v165, 0
	s_mov_b64 s[38:39], -1
	s_mov_b32 s49, 0
	v_mov_b64_e32 v[76:77], v[12:13]
	v_mov_b64_e32 v[74:75], v[10:11]
	v_mov_b64_e32 v[72:73], v[8:9]
	v_mov_b64_e32 v[70:71], v[6:7]
	v_mov_b64_e32 v[68:69], v[4:5]
	v_mov_b64_e32 v[66:67], v[2:3]
	v_mov_b64_e32 v[64:65], v[0:1]
	v_mov_b64_e32 v[60:61], v[12:13]
	v_mov_b64_e32 v[58:59], v[10:11]
	v_mov_b64_e32 v[56:57], v[8:9]
	v_mov_b64_e32 v[54:55], v[6:7]
	v_mov_b64_e32 v[52:53], v[4:5]
	v_mov_b64_e32 v[50:51], v[2:3]
	v_mov_b64_e32 v[48:49], v[0:1]
	v_mov_b64_e32 v[44:45], v[12:13]
	v_mov_b64_e32 v[42:43], v[10:11]
	v_mov_b64_e32 v[40:41], v[8:9]
	v_mov_b64_e32 v[38:39], v[6:7]
	v_mov_b64_e32 v[36:37], v[4:5]
	v_mov_b64_e32 v[34:35], v[2:3]
	v_mov_b64_e32 v[32:33], v[0:1]
	v_mov_b64_e32 v[28:29], v[12:13]
	v_mov_b64_e32 v[26:27], v[10:11]
	v_mov_b64_e32 v[24:25], v[8:9]
	v_mov_b64_e32 v[22:23], v[6:7]
	v_mov_b64_e32 v[20:21], v[4:5]
	v_mov_b64_e32 v[18:19], v[2:3]
	v_mov_b64_e32 v[16:17], v[0:1]
	v_mov_b64_e32 v[92:93], v[12:13]
	v_mov_b64_e32 v[90:91], v[10:11]
	v_mov_b64_e32 v[88:89], v[8:9]
	v_mov_b64_e32 v[86:87], v[6:7]
	v_mov_b64_e32 v[84:85], v[4:5]
	v_mov_b64_e32 v[82:83], v[2:3]
	v_mov_b64_e32 v[80:81], v[0:1]
	s_mov_b32 s94, 0
	s_waitcnt vmcnt(0)
	s_mul_hi_u32 s57, s79, 0xaaaaaaab
	s_lshr_b32 s57, s57, 1
	s_mul_i32 s57, s57, 0x18000
	s_sub_i32 s58, s60, s57
	s_sub_i32 s59, s61, s57
	s_add_i32 s58, s49, s58
	v_lshl_add_u64 v[2:3], v[150:151], 0, s[52:53]
	s_sub_i32 s80, s4, s57
	s_add_i32 m0, s90, s58
	v_lshl_add_u64 v[4:5], v[2:3], 0, s[36:37]
	s_add_i32 s58, s49, s59
	s_sub_i32 s57, s5, s57
	global_load_lds_dwordx4 v[4:5], off
	v_lshl_add_u64 v[4:5], v[148:149], 0, s[52:53]
	s_add_i32 m0, s90, s58
	s_add_i32 s58, s49, s80
	global_load_lds_dwordx4 v[4:5], off
	v_lshl_add_u64 v[2:3], v[2:3], 0, s[24:25]
	s_add_i32 m0, s90, s58
	s_add_i32 s57, s49, s57
	global_load_lds_dwordx4 v[2:3], off
	v_lshl_add_u64 v[2:3], v[146:147], 0, s[52:53]
	s_add_i32 m0, s90, s57
	s_nop 0
	global_load_lds_dwordx4 v[2:3], off
	v_lshl_add_u64 v[146:147], v[146:147], 0, s[68:69]
	v_lshl_add_u64 v[148:149], v[148:149], 0, s[68:69]
	v_lshl_add_u64 v[150:151], v[150:151], 0, s[68:69]
	ds_read_b128 v[2:5], v161
	ds_read_b128 v[6:9], v161 offset:8192
	ds_read_b128 v[10:13], v162
	ds_read_b128 v[166:169], v162 offset:8192
	ds_read_b128 v[186:189], v163
	ds_read_b128 v[190:193], v163 offset:8192
	ds_read_b128 v[218:221], v164
	ds_read_b128 v[222:225], v164 offset:8192
	s_cmp_le_u32 s48, s88
	s_cselect_b64 vcc, -1, 0
	s_waitcnt lgkmcnt(0)
	v_cndmask_b32_e32 v15, 0, v158, vcc
	v_sub_f32_e32 v96, v15, v165
	v_mov_b32_e32 v97, v96
	v_mov_b32_e32 v98, v96
	v_mov_b32_e32 v99, v96
	v_mov_b32_e32 v100, v96
	v_mov_b32_e32 v101, v96
	v_mov_b32_e32 v102, v96
	v_mov_b32_e32 v103, v96
	v_mov_b32_e32 v104, v96
	v_mov_b32_e32 v105, v96
	v_mov_b32_e32 v106, v96
	v_mov_b32_e32 v107, v96
	v_mov_b32_e32 v108, v96
	v_mov_b32_e32 v109, v96
	v_mov_b32_e32 v110, v96
	v_mov_b32_e32 v111, v96
	s_nop 1
	v_mfma_f32_32x32x16_bf16 v[112:127], v[2:5], v[128:131], v[96:111]
	v_mfma_f32_32x32x16_bf16 v[96:111], v[6:9], v[128:131], v[96:111]
	v_mfma_f32_32x32x16_bf16 v[112:127], v[10:13], v[132:135], v[112:127]
	v_mfma_f32_32x32x16_bf16 v[96:111], v[166:169], v[132:135], v[96:111]
	v_mfma_f32_32x32x16_bf16 v[112:127], v[186:189], v[136:139], v[112:127]
	v_mfma_f32_32x32x16_bf16 v[96:111], v[190:193], v[136:139], v[96:111]
	v_mfma_f32_32x32x16_bf16 v[112:127], v[218:221], v[140:143], v[112:127]
	v_mfma_f32_32x32x16_bf16 v[96:111], v[222:225], v[140:143], v[96:111]
	s_branch .LBB0_787

; #define LAS __attribute__((address_space(3)))
; #define MFMA32(a, b, c) __builtin_amdgcn_mfma_f32_32x32x16_bf16((a), (b), (c), 0, 0, 0)
;     __device__ __forceinline__ void init(const void* A_, const void* B_, int lda_, int ldb_, int M, unsigned mask_, int G_, int c_) { A = (const char*)A_; B = (const char*)B_; lda = lda_; ldb = ldb_; nM = M / BM; mask = mask_; nN = __builtin_popcount(mask_); nwg = nM * nN; G = G_; c = c_; }
;     __device__ __forceinline__ void init(f32x4 (&acc)[2][2][4][2], const Unit& u, int wr, int wc, int fr, int fq) const { u32x4 old[2][4][2]; init_load(old, u, wr, wc, fr, fq); init_finish(acc, old); }
; template <int KS> DI void at_qk(f32x16& p0, f32x16& p1, LAS const unsigned char* Kt, int mapB, const bf16x8 (&qr)[8], float init, int r32, int hi) {
; #pragma unroll
;     for (int i = 0; i < 16; ++i) { p0[i] = init; p1[i] = init; }
;     bf16x8 kb[KS][2];
; #pragma unroll
;     for (int d0 = 0; d0 < KS; ++d0) { const int cb = mapB + (d0 * 16 + hi * 8) * 2;
;         kb[d0][0] = *(const LAS bf16x8*)(Kt + AT_KSWZ(r32, cb)); kb[d0][1] = *(const LAS bf16x8*)(Kt + AT_KSWZ(32 + r32, cb)); }
;     __builtin_amdgcn_sched_barrier(0);
; #pragma unroll
;     for (int d0 = 0; d0 < KS; ++d0) { p0 = MFMA32(kb[d0][0], qr[d0], p0); p1 = MFMA32(kb[d0][1], qr[d0], p1); }
; DI float at_softmax(f32x16& p0, f32x16& p1, float& m_run, bool first, bool nearb, LAS const float* tabp, int lane) {
;     if (nearb) {
; #pragma unroll
;         for (int i = 0; i < 16; ++i) { p0[i] += tabp[8 * (i >> 2) + (i & 3)]; p1[i] += tabp[32 + 8 * (i >> 2) + (i & 3)]; }
;     }
;     float mx = p0[0];
; #pragma unroll
;     for (int i = 1; i < 16; ++i) mx = fmaxf(mx, p0[i]);
; #pragma unroll
;     for (int i = 0; i < 16; ++i) mx = fmaxf(mx, p1[i]);
.LBB0_794:
	v_add_u32_e32 v0, s100, v161
	ds_read_b128 v[2:5], v0
	ds_read_b128 v[6:9], v0 offset:8192
	v_add_u32_e32 v0, s100, v162
	ds_read_b128 v[10:13], v0
	ds_read_b128 v[166:169], v0 offset:8192
	v_add_u32_e32 v0, s100, v163
	ds_read_b128 v[186:189], v0
	ds_read_b128 v[190:193], v0 offset:8192
	v_add_u32_e32 v0, s100, v164
	ds_read_b128 v[218:221], v0
	ds_read_b128 v[222:225], v0 offset:8192
	s_add_i32 s101, s48, 64
	s_cmp_le_u32 s101, s88
	s_cselect_b64 vcc, -1, 0
	v_cndmask_b32_e32 v15, 0, v158, vcc
	v_sub_f32_e32 v232, v15, v165
	v_mov_b32_e32 v233, v232
	v_mov_b32_e32 v234, v232
	v_mov_b32_e32 v235, v232
	v_mov_b32_e32 v236, v232
	v_mov_b32_e32 v237, v232
	v_mov_b32_e32 v238, v232
	v_mov_b32_e32 v239, v232
	v_mov_b32_e32 v240, v232
	v_mov_b32_e32 v241, v232
	v_mov_b32_e32 v242, v232
	v_mov_b32_e32 v243, v232
	v_mov_b32_e32 v244, v232
	v_mov_b32_e32 v245, v232
	v_mov_b32_e32 v246, v232
	v_mov_b32_e32 v247, v232
	v_max_f32_e32 v0, v113, v113
	v_max_f32_e32 v14, v112, v112
	v_max_f32_e32 v0, v14, v0
	v_max3_f32 v0, v0, v114, v115
	v_max3_f32 v0, v0, v116, v117
	s_waitcnt lgkmcnt(0)
	v_mfma_f32_32x32x16_bf16 v[202:217], v[2:5], v[128:131], v[232:247]
	v_max3_f32 v0, v0, v118, v119
	v_max3_f32 v0, v0, v120, v121
	v_mfma_f32_32x32x16_bf16 v[232:247], v[6:9], v[128:131], v[232:247]
	v_max3_f32 v0, v0, v122, v123
	v_max3_f32 v0, v0, v124, v125
	v_mfma_f32_32x32x16_bf16 v[202:217], v[10:13], v[132:135], v[202:217]
	v_max3_f32 v0, v0, v126, v127
	v_max3_f32 v0, v0, v96, v97
	v_mfma_f32_32x32x16_bf16 v[232:247], v[166:169], v[132:135], v[232:247]
	v_max3_f32 v0, v0, v98, v99
	v_max3_f32 v0, v0, v100, v101
	v_mfma_f32_32x32x16_bf16 v[202:217], v[186:189], v[136:139], v[202:217]
	v_max3_f32 v0, v0, v102, v103
	v_max3_f32 v0, v0, v104, v105
	v_mfma_f32_32x32x16_bf16 v[232:247], v[190:193], v[136:139], v[232:247]
	v_max3_f32 v0, v0, v106, v107
	v_max3_f32 v0, v0, v108, v109
	s_xor_b64 s[58:59], s[38:39], -1
	v_max3_f32 v2, v0, v110, v111
	s_and_b64 vcc, exec, s[58:59]
	s_cbranch_vccz .LBB0_796
	s_mov_b32 s58, 0x41000000
	v_cmp_ge_f32_e32 vcc, s58, v2
	s_cmp_lg_u64 vcc, exec
	s_cselect_b64 s[58:59], -1, 0
	s_cbranch_execz .LBB0_797
	s_branch .LBB0_798

; #define MFMA32(a, b, c) __builtin_amdgcn_mfma_f32_32x32x16_bf16((a), (b), (c), 0, 0, 0)
; template <int OFF> DI s16x4 at_tr_read(int vb) { s16x4 r; asm volatile("ds_read_b64_tr_b16 %0, %1 offset:%2" : "=&v"(r) : "v"(vb), "i"(OFF) : "memory"); return r; }
; DI unsigned at_cvtpk(float lo, float hi) { unsigned r; asm volatile("v_cvt_pk_bf16_f32 %0, %1, %2" : "=v"(r) : "v"(lo), "v"(hi)); return r; }
; DI float at_softmax(f32x16& p0, f32x16& p1, float& m_run, bool first, bool nearb, LAS const float* tabp, int lane) {
;     ...
;     for (int i = 0; i < 16; ++i) p0[i] = __builtin_amdgcn_exp2f(p0[i]);
; #pragma unroll
;     for (int i = 0; i < 16; ++i) p1[i] = __builtin_amdgcn_exp2f(p1[i]);
;     return alpha;
; }
; DI bf16x8 at_pack(const f32x16& p, int s8) {
;     u32x4 w; w.x = at_cvtpk(p[s8], p[s8 + 1]); w.y = at_cvtpk(p[s8 + 2], p[s8 + 3]); w.z = at_cvtpk(p[s8 + 4], p[s8 + 5]); w.w = at_cvtpk(p[s8 + 6], p[s8 + 7]);
;     return __builtin_bit_cast(bf16x8, w);
; }
; template <int D0> DI void at_pv_block(f32x16 (&o)[4], int vb, const bf16x8 (&pf)[4]) {
;     const s16x4 l0 = at_tr_read<D0 * 512 + 0 * 4096>(vb), h0 = at_tr_read<D0 * 512 + 0 * 4096 + 2048>(vb), l1 = at_tr_read<D0 * 512 + 1 * 4096>(vb), h1 = at_tr_read<D0 * 512 + 1 * 4096 + 2048>(vb);
;     const s16x4 l2 = at_tr_read<D0 * 512 + 2 * 4096>(vb), h2 = at_tr_read<D0 * 512 + 2 * 4096 + 2048>(vb), l3 = at_tr_read<D0 * 512 + 3 * 4096>(vb), h3 = at_tr_read<D0 * 512 + 3 * 4096 + 2048>(vb);
;     asm volatile("s_waitcnt lgkmcnt(0)" ::: "memory"); __builtin_amdgcn_sched_barrier(0);
;     ...
;     o[D0] = MFMA32(AT_PK(l0, h0), pf[0], o[D0]); o[D0] = MFMA32(AT_PK(l1, h1), pf[1], o[D0]); o[D0] = MFMA32(AT_PK(l2, h2), pf[2], o[D0]); o[D0] = MFMA32(AT_PK(l3, h3), pf[3], o[D0]);
; DI void attn_unit_diff(const Ctx& C, int l, int b, int h, int j) {
;     ...
;             pf[0] = at_pack(p0, 0); pf[1] = at_pack(p0, 8); pf[2] = at_pack(p1, 0); pf[3] = at_pack(p1, 8);
;             ol = MFMA32(ones, pf[0], ol); ol = MFMA32(ones, pf[1], ol); ol = MFMA32(ones, pf[2], ol); ol = MFMA32(ones, pf[3], ol);
;             at_pv_block<0>(o, vb, pf); at_pv_block<1>(o, vb, pf); at_pv_block<2>(o, vb, pf); at_pv_block<3>(o, vb, pf);
.LBB0_801:
	v_subrev_u32_e32 v87, s57, v160
	v_add_u32_e32 v87, s49, v87
	ds_read_b64_tr_b16 v[170:171], v87 offset:0x0
	ds_read_b64_tr_b16 v[172:173], v87 offset:0x800
	ds_read_b64_tr_b16 v[174:175], v87 offset:0x200
	ds_read_b64_tr_b16 v[176:177], v87 offset:0xa00
	ds_read_b64_tr_b16 v[178:179], v87 offset:0x400
	ds_read_b64_tr_b16 v[180:181], v87 offset:0xc00
	ds_read_b64_tr_b16 v[182:183], v87 offset:0x600
	ds_read_b64_tr_b16 v[184:185], v87 offset:0xe00
	v_exp_f32_e32 v112, v112
	v_exp_f32_e32 v113, v113
	v_mfma_f32_32x32x16_bf16 v[202:217], v[218:221], v[140:143], v[202:217]
	v_exp_f32_e32 v114, v114
	v_exp_f32_e32 v115, v115
	v_mfma_f32_32x32x16_bf16 v[232:247], v[222:225], v[140:143], v[232:247]
	v_exp_f32_e32 v116, v116
	v_exp_f32_e32 v117, v117
	v_exp_f32_e32 v118, v118
	v_exp_f32_e32 v119, v119
	v_cvt_pk_bf16_f32 v2, v112, v113
	v_cvt_pk_bf16_f32 v3, v114, v115
	v_cvt_pk_bf16_f32 v4, v116, v117
	v_cvt_pk_bf16_f32 v5, v118, v119
	v_add_f32_e32 v81, v112, v113
	v_add_f32_e32 v82, v114, v115
	v_add_f32_e32 v83, v116, v117
	v_add_f32_e32 v84, v118, v119
	v_add_f32_e32 v81, v81, v82
	v_add_f32_e32 v83, v83, v84
	v_add_f32_e32 v81, v81, v83
	v_add_f32_e32 v80, v80, v81
	s_waitcnt lgkmcnt(0)
	ds_read_b64_tr_b16 v[112:113], v87 offset:0x1000
	ds_read_b64_tr_b16 v[114:115], v87 offset:0x1800
	ds_read_b64_tr_b16 v[116:117], v87 offset:0x1200
	ds_read_b64_tr_b16 v[118:119], v87 offset:0x1a00
	ds_read_b64_tr_b16 v[88:89], v87 offset:0x1400
	ds_read_b64_tr_b16 v[90:91], v87 offset:0x1c00
	ds_read_b64_tr_b16 v[92:93], v87 offset:0x1600
	ds_read_b64_tr_b16 v[94:95], v87 offset:0x1e00
	v_mfma_f32_32x32x16_bf16 v[64:79], v[170:173], v[2:5], v[64:79]
	v_exp_f32_e32 v120, v120
	v_exp_f32_e32 v121, v121
	v_mfma_f32_32x32x16_bf16 v[48:63], v[174:177], v[2:5], v[48:63]
	v_exp_f32_e32 v122, v122
	v_exp_f32_e32 v123, v123
	v_mfma_f32_32x32x16_bf16 v[32:47], v[178:181], v[2:5], v[32:47]
	v_exp_f32_e32 v124, v124
	v_exp_f32_e32 v125, v125
	v_mfma_f32_32x32x16_bf16 v[16:31], v[182:185], v[2:5], v[16:31]
	v_exp_f32_e32 v126, v126
	v_exp_f32_e32 v127, v127
	v_cvt_pk_bf16_f32 v6, v120, v121
	v_cvt_pk_bf16_f32 v7, v122, v123
	v_cvt_pk_bf16_f32 v8, v124, v125
	v_cvt_pk_bf16_f32 v9, v126, v127
	v_add_f32_e32 v81, v120, v121
	v_add_f32_e32 v82, v122, v123
	v_add_f32_e32 v83, v124, v125
	v_add_f32_e32 v84, v126, v127
	v_add_f32_e32 v81, v81, v82
	v_add_f32_e32 v83, v83, v84
	v_add_f32_e32 v81, v81, v83
	v_add_f32_e32 v80, v80, v81
	s_waitcnt lgkmcnt(0)
	ds_read_b64_tr_b16 v[170:171], v87 offset:0x2000
	ds_read_b64_tr_b16 v[172:173], v87 offset:0x2800
	ds_read_b64_tr_b16 v[174:175], v87 offset:0x2200
	ds_read_b64_tr_b16 v[176:177], v87 offset:0x2a00
	ds_read_b64_tr_b16 v[178:179], v87 offset:0x2400
	ds_read_b64_tr_b16 v[180:181], v87 offset:0x2c00
	ds_read_b64_tr_b16 v[182:183], v87 offset:0x2600
	ds_read_b64_tr_b16 v[184:185], v87 offset:0x2e00
	v_mfma_f32_32x32x16_bf16 v[64:79], v[112:115], v[6:9], v[64:79]
	v_exp_f32_e32 v96, v96
	v_exp_f32_e32 v97, v97
	v_mfma_f32_32x32x16_bf16 v[48:63], v[116:119], v[6:9], v[48:63]
	v_exp_f32_e32 v98, v98
	v_exp_f32_e32 v99, v99
	v_mfma_f32_32x32x16_bf16 v[32:47], v[88:91], v[6:9], v[32:47]
	v_exp_f32_e32 v100, v100
	v_exp_f32_e32 v101, v101
	v_mfma_f32_32x32x16_bf16 v[16:31], v[92:95], v[6:9], v[16:31]
	v_exp_f32_e32 v102, v102
	v_exp_f32_e32 v103, v103
	v_cvt_pk_bf16_f32 v10, v96, v97
	v_cvt_pk_bf16_f32 v11, v98, v99
	v_cvt_pk_bf16_f32 v12, v100, v101
	v_cvt_pk_bf16_f32 v13, v102, v103
	v_add_f32_e32 v81, v96, v97
	v_add_f32_e32 v82, v98, v99
	v_add_f32_e32 v83, v100, v101
	v_add_f32_e32 v84, v102, v103
	v_add_f32_e32 v81, v81, v82
	v_add_f32_e32 v83, v83, v84
	v_add_f32_e32 v81, v81, v83
	v_add_f32_e32 v80, v80, v81
	s_waitcnt lgkmcnt(0)
	ds_read_b64_tr_b16 v[112:113], v87 offset:0x3000
	ds_read_b64_tr_b16 v[114:115], v87 offset:0x3800
	ds_read_b64_tr_b16 v[116:117], v87 offset:0x3200
	ds_read_b64_tr_b16 v[118:119], v87 offset:0x3a00
	ds_read_b64_tr_b16 v[88:89], v87 offset:0x3400
	ds_read_b64_tr_b16 v[90:91], v87 offset:0x3c00
	ds_read_b64_tr_b16 v[92:93], v87 offset:0x3600
	ds_read_b64_tr_b16 v[94:95], v87 offset:0x3e00
	v_mfma_f32_32x32x16_bf16 v[64:79], v[170:173], v[10:13], v[64:79]
	v_exp_f32_e32 v104, v104
	v_exp_f32_e32 v105, v105
	v_mfma_f32_32x32x16_bf16 v[48:63], v[174:177], v[10:13], v[48:63]
	v_exp_f32_e32 v106, v106
	v_exp_f32_e32 v107, v107
	v_mfma_f32_32x32x16_bf16 v[32:47], v[178:181], v[10:13], v[32:47]
	v_exp_f32_e32 v108, v108
	v_exp_f32_e32 v109, v109
	v_mfma_f32_32x32x16_bf16 v[16:31], v[182:185], v[10:13], v[16:31]
	v_exp_f32_e32 v110, v110
	v_exp_f32_e32 v111, v111
	v_cvt_pk_bf16_f32 v166, v104, v105
	v_cvt_pk_bf16_f32 v167, v106, v107
	v_cvt_pk_bf16_f32 v168, v108, v109
	v_cvt_pk_bf16_f32 v169, v110, v111
	v_add_f32_e32 v81, v104, v105
	v_add_f32_e32 v82, v106, v107
	v_add_f32_e32 v83, v108, v109
	v_add_f32_e32 v84, v110, v111
	v_add_f32_e32 v81, v81, v82
	v_add_f32_e32 v83, v83, v84
	v_add_f32_e32 v81, v81, v83
	v_add_f32_e32 v80, v80, v81
	s_waitcnt lgkmcnt(0)
	v_mfma_f32_32x32x16_bf16 v[64:79], v[112:115], v[166:169], v[64:79]
	v_mov_b64_e32 v[96:97], v[232:233]
	v_mov_b64_e32 v[98:99], v[234:235]
	v_mov_b64_e32 v[100:101], v[236:237]
	v_mov_b64_e32 v[102:103], v[238:239]
	v_mfma_f32_32x32x16_bf16 v[48:63], v[116:119], v[166:169], v[48:63]
	v_mov_b64_e32 v[104:105], v[240:241]
	v_mov_b64_e32 v[106:107], v[242:243]
	v_mov_b64_e32 v[108:109], v[244:245]
	v_mov_b64_e32 v[110:111], v[246:247]
	v_mfma_f32_32x32x16_bf16 v[32:47], v[88:91], v[166:169], v[32:47]
	v_mov_b64_e32 v[120:121], v[210:211]
	v_mov_b64_e32 v[122:123], v[212:213]
	v_mov_b64_e32 v[124:125], v[214:215]
	v_mov_b64_e32 v[126:127], v[216:217]
	v_mfma_f32_32x32x16_bf16 v[16:31], v[92:95], v[166:169], v[16:31]
	v_mov_b64_e32 v[112:113], v[202:203]
	v_mov_b64_e32 v[114:115], v[204:205]
	v_mov_b64_e32 v[116:117], v[206:207]
	v_mov_b64_e32 v[118:119], v[208:209]
	s_mov_b64 s[38:39], 0
	s_mov_b64 s[58:59], -1
	s_and_b64 vcc, exec, s[40:41]
	s_cbranch_vccz .LBB0_790

; DI float max_x32(float v, int lane) { return fmaxf(v, bpx(v, lane, 32)); }
; DI float at_softmax(f32x16& p0, f32x16& p1, float& m_run, bool first, bool nearb, LAS const float* tabp, int lane) {
;     ...
;     if (first || !__all(mx <= AT_THR)) {
;         mx = max_x32(mx, lane);
;         const float dl = first ? mx : fmaxf(mx, 0.f);
;         alpha = first ? 1.f : __builtin_amdgcn_exp2f(-dl); m_run += dl;
; #pragma unroll
;         for (int i = 0; i < 16; ++i) { p0[i] -= dl; p1[i] -= dl; }
;     }
.LBB0_804:
	ds_bpermute_b32 v0, v157, v2
	v_max_f32_e32 v2, v2, v2
	s_waitcnt lgkmcnt(0)
	v_max_f32_e32 v0, v0, v0
	v_max_f32_e32 v0, v2, v0
	v_max_f32_e32 v2, 0, v0
	v_cndmask_b32_e64 v0, v2, v0, s[38:39]
	v_exp_f32_e64 v2, -v0
	v_add_f32_e32 v165, v165, v0
	v_pk_add_f32 v[112:113], v[112:113], v[0:1] op_sel_hi:[1,0] neg_lo:[0,1] neg_hi:[0,1]
	v_pk_add_f32 v[96:97], v[96:97], v[0:1] op_sel_hi:[1,0] neg_lo:[0,1] neg_hi:[0,1]
	v_pk_add_f32 v[114:115], v[114:115], v[0:1] op_sel_hi:[1,0] neg_lo:[0,1] neg_hi:[0,1]
	v_pk_add_f32 v[98:99], v[98:99], v[0:1] op_sel_hi:[1,0] neg_lo:[0,1] neg_hi:[0,1]
	v_pk_add_f32 v[116:117], v[116:117], v[0:1] op_sel_hi:[1,0] neg_lo:[0,1] neg_hi:[0,1]
	v_pk_add_f32 v[100:101], v[100:101], v[0:1] op_sel_hi:[1,0] neg_lo:[0,1] neg_hi:[0,1]
	v_pk_add_f32 v[118:119], v[118:119], v[0:1] op_sel_hi:[1,0] neg_lo:[0,1] neg_hi:[0,1]
	v_pk_add_f32 v[102:103], v[102:103], v[0:1] op_sel_hi:[1,0] neg_lo:[0,1] neg_hi:[0,1]
	v_pk_add_f32 v[120:121], v[120:121], v[0:1] op_sel_hi:[1,0] neg_lo:[0,1] neg_hi:[0,1]
	v_pk_add_f32 v[104:105], v[104:105], v[0:1] op_sel_hi:[1,0] neg_lo:[0,1] neg_hi:[0,1]
	v_pk_add_f32 v[122:123], v[122:123], v[0:1] op_sel_hi:[1,0] neg_lo:[0,1] neg_hi:[0,1]
	v_pk_add_f32 v[106:107], v[106:107], v[0:1] op_sel_hi:[1,0] neg_lo:[0,1] neg_hi:[0,1]
	v_pk_add_f32 v[124:125], v[124:125], v[0:1] op_sel_hi:[1,0] neg_lo:[0,1] neg_hi:[0,1]
	v_pk_add_f32 v[108:109], v[108:109], v[0:1] op_sel_hi:[1,0] neg_lo:[0,1] neg_hi:[0,1]
	v_pk_add_f32 v[126:127], v[126:127], v[0:1] op_sel_hi:[1,0] neg_lo:[0,1] neg_hi:[0,1]
	v_pk_add_f32 v[110:111], v[110:111], v[0:1] op_sel_hi:[1,0] neg_lo:[0,1] neg_hi:[0,1]
	s_nop 15
	v_pk_add_f32 v[202:203], v[202:203], v[0:1] op_sel_hi:[1,0] neg_lo:[0,1] neg_hi:[0,1]
	v_pk_add_f32 v[204:205], v[204:205], v[0:1] op_sel_hi:[1,0] neg_lo:[0,1] neg_hi:[0,1]
	v_pk_add_f32 v[206:207], v[206:207], v[0:1] op_sel_hi:[1,0] neg_lo:[0,1] neg_hi:[0,1]
	v_pk_add_f32 v[208:209], v[208:209], v[0:1] op_sel_hi:[1,0] neg_lo:[0,1] neg_hi:[0,1]
	v_pk_add_f32 v[210:211], v[210:211], v[0:1] op_sel_hi:[1,0] neg_lo:[0,1] neg_hi:[0,1]
	v_pk_add_f32 v[212:213], v[212:213], v[0:1] op_sel_hi:[1,0] neg_lo:[0,1] neg_hi:[0,1]
	v_pk_add_f32 v[214:215], v[214:215], v[0:1] op_sel_hi:[1,0] neg_lo:[0,1] neg_hi:[0,1]
	v_pk_add_f32 v[216:217], v[216:217], v[0:1] op_sel_hi:[1,0] neg_lo:[0,1] neg_hi:[0,1]
	v_pk_add_f32 v[232:233], v[232:233], v[0:1] op_sel_hi:[1,0] neg_lo:[0,1] neg_hi:[0,1]
	v_pk_add_f32 v[234:235], v[234:235], v[0:1] op_sel_hi:[1,0] neg_lo:[0,1] neg_hi:[0,1]
	v_pk_add_f32 v[236:237], v[236:237], v[0:1] op_sel_hi:[1,0] neg_lo:[0,1] neg_hi:[0,1]
	v_pk_add_f32 v[238:239], v[238:239], v[0:1] op_sel_hi:[1,0] neg_lo:[0,1] neg_hi:[0,1]
	v_pk_add_f32 v[240:241], v[240:241], v[0:1] op_sel_hi:[1,0] neg_lo:[0,1] neg_hi:[0,1]
	v_pk_add_f32 v[242:243], v[242:243], v[0:1] op_sel_hi:[1,0] neg_lo:[0,1] neg_hi:[0,1]
	v_pk_add_f32 v[244:245], v[244:245], v[0:1] op_sel_hi:[1,0] neg_lo:[0,1] neg_hi:[0,1]
	v_pk_add_f32 v[246:247], v[246:247], v[0:1] op_sel_hi:[1,0] neg_lo:[0,1] neg_hi:[0,1]
	v_cndmask_b32_e64 v0, v2, 1.0, s[38:39]
	v_cmp_neq_f32_e32 vcc, 1.0, v0
	s_cbranch_vccnz .LBB0_800
	s_branch .LBB0_801

; #define LAS __attribute__((address_space(3)))
; #define MFMA32(a, b, c) __builtin_amdgcn_mfma_f32_32x32x16_bf16((a), (b), (c), 0, 0, 0)
; DI int at_v_rd_base(int lane) { return ((lane & 3) << 3) | (((lane >> 2) & 3) << 6) | (((lane >> 4) & 1) << 5) | (((lane >> 5) & 1) << 8); }
;     __device__ __forceinline__ void init(const void* A_, const void* B_, int lda_, int ldb_, int M, unsigned mask_, int G_, int c_) { A = (const char*)A_; B = (const char*)B_; lda = lda_; ldb = ldb_; nM = M / BM; mask = mask_; nN = __builtin_popcount(mask_); nwg = nM * nN; G = G_; c = c_; }
; template <int KS> DI void at_qk(f32x16& p0, f32x16& p1, LAS const unsigned char* Kt, int mapB, const bf16x8 (&qr)[8], float init, int r32, int hi) {
; #pragma unroll
;     for (int i = 0; i < 16; ++i) { p0[i] = init; p1[i] = init; }
;     bf16x8 kb[KS][2];
; #pragma unroll
;     for (int d0 = 0; d0 < KS; ++d0) { const int cb = mapB + (d0 * 16 + hi * 8) * 2;
;         kb[d0][0] = *(const LAS bf16x8*)(Kt + AT_KSWZ(r32, cb)); kb[d0][1] = *(const LAS bf16x8*)(Kt + AT_KSWZ(32 + r32, cb)); }
;     __builtin_amdgcn_sched_barrier(0);
; #pragma unroll
;     for (int d0 = 0; d0 < KS; ++d0) { p0 = MFMA32(kb[d0][0], qr[d0], p0); p1 = MFMA32(kb[d0][1], qr[d0], p1); }
; DI void attn_unit_diff(const Ctx& C, int l, int b, int h, int j) {
;     ...
;     f32x16 o[4], ol = {}; float m_run = 0.f; bool first = true;
; #pragma unroll
;     for (int d0 = 0; d0 < 4; ++d0) o[d0] = f32x16{};
;     const bf16x8 ones = {16256, 16256, 16256, 16256, 16256, 16256, 16256, 16256};
;     asm volatile("s_waitcnt vmcnt(0) lgkmcnt(0)\n\ts_barrier" ::: "memory");
;     const float cfar = tabl[0];
;     const int vrd = at_v_rd_base(lane);
;     for (int sd = 0; sd < nt; ++sd) {
;         const int slot = sd % 3;
;         const bool staged = sd + 2 < nt;
;         if (staged) at_stage1(C.lds, projb, kcolB, vcolB, sd + 2, (sd + 2) % 3, wid, lb0, lb1);
;         if (sd <= cw) {
;             LAS const unsigned char* Kt = C.lds + slot * 32768;
;             const int vb = (int)(size_t)(Kt + 16384) + vrd;
;             const bool nearb = (sd * 64 + 63 - q0w) > -305;
;             LAS const float* tabp = tabl + (sd * 64 - qpos + TABB_OFF + 4 * hi);
;             f32x16 p0, p1;
;             at_qk<KS>(p0, p1, Kt, g * 128, qr, (nearb ? 0.f : cfar) - m_run, r32, hi);
.LBB0_828:
	s_or_b64 exec, exec, s[58:59]
	s_and_b32 s11, s22, 15
	s_waitcnt vmcnt(0) lgkmcnt(0)
	s_barrier
	v_mov_b32_e32 v4, s50
	s_lshl_b32 s6, s6, 1
	v_readlane_b32 s7, v252, 22
	s_lshl_b32 s31, s11, 7
	s_lshl_b32 s11, s11, 16
	s_waitcnt lgkmcnt(0)
	ds_read_b32 v158, v4
	v_and_b32_e32 v4, 24, v8
	v_and_b32_e32 v7, 0x100, v8
	v_lshlrev_b32_e32 v8, 4, v156
	v_readlane_b32 s15, v252, 26
	v_readlane_b32 s35, v252, 23
	v_mov_b32_e32 v3, v1
	s_or_b32 s7, s6, s7
	s_add_i32 s11, s11, 0x10000
	v_lshlrev_b32_e32 v145, 4, v154
	v_add_u32_e32 v9, s15, v8
	v_lshlrev_b32_e32 v11, 4, v155
	v_lshlrev_b32_e32 v15, 2, v154
	s_add_i32 s16, s55, 0xfffffe90
	s_or_b32 s31, s35, s31
	s_add_i32 s52, s48, s28
	v_and_b32_e32 v5, 0xc0, v145
	v_lshlrev_b32_e32 v6, 1, v154
	v_lshlrev_b32_e32 v10, 8, v155
	v_and_b32_e32 v11, 0x70, v11
	v_add_u32_e32 v14, 0x60, v9
	v_xor_b32_e32 v157, 0x80, v15
	v_add_lshl_u32 v15, s31, v155, 2
	v_lshl_add_u64 v[2:3], s[42:43], 0, v[2:3]
	s_add_u32 s42, s96, s42
	v_and_b32_e32 v6, 32, v6
	v_add_u32_e32 v12, 32, v9
	v_add_u32_e32 v13, 64, v9
	v_sub_u32_e32 v159, v8, v15
	v_add3_u32 v5, v7, s91, v5
	v_xad_u32 v164, v14, v11, v10
	s_addc_u32 s43, s89, s43
	v_mov_b32_e32 v14, v1
	v_mov_b32_e32 v15, v1
	v_add3_u32 v160, v5, v6, v4
	v_xad_u32 v161, v9, v11, v10
	v_xad_u32 v162, v12, v11, v10
	v_xad_u32 v163, v13, v11, v10
	v_lshl_add_u64 v[146:147], s[70:71], 0, v[2:3]
	v_lshl_add_u64 v[148:149], s[72:73], 0, v[2:3]
	v_lshl_add_u64 v[150:151], s[42:43], 0, v[0:1]
	v_mov_b32_e32 v0, v1
	v_mov_b32_e32 v2, v1
	v_mov_b32_e32 v3, v1
	v_mov_b32_e32 v4, v1
	v_mov_b32_e32 v5, v1
	v_mov_b32_e32 v6, v1
	v_mov_b32_e32 v7, v1
	v_mov_b32_e32 v8, v1
	v_mov_b32_e32 v9, v1
	v_mov_b32_e32 v10, v1
	v_mov_b32_e32 v11, v1
	v_mov_b32_e32 v12, v1
	v_mov_b32_e32 v13, v1
	v_mov_b64_e32 v[78:79], v[14:15]
	v_mov_b64_e32 v[62:63], v[14:15]
	v_mov_b64_e32 v[46:47], v[14:15]
	v_mov_b64_e32 v[30:31], v[14:15]
	v_mov_b64_e32 v[94:95], v[14:15]
	s_mov_b32 s15, 2
	s_mov_b32 s28, 0
	v_mov_b32_e32 v165, 0
	s_mov_b64 s[42:43], -1
	s_mov_b32 s31, 0
	v_mov_b64_e32 v[76:77], v[12:13]
	v_mov_b64_e32 v[74:75], v[10:11]
	v_mov_b64_e32 v[72:73], v[8:9]
	v_mov_b64_e32 v[70:71], v[6:7]
	v_mov_b64_e32 v[68:69], v[4:5]
	v_mov_b64_e32 v[66:67], v[2:3]
	v_mov_b64_e32 v[64:65], v[0:1]
	v_mov_b64_e32 v[60:61], v[12:13]
	v_mov_b64_e32 v[58:59], v[10:11]
	v_mov_b64_e32 v[56:57], v[8:9]
	v_mov_b64_e32 v[54:55], v[6:7]
	v_mov_b64_e32 v[52:53], v[4:5]
	v_mov_b64_e32 v[50:51], v[2:3]
	v_mov_b64_e32 v[48:49], v[0:1]
	v_mov_b64_e32 v[44:45], v[12:13]
	v_mov_b64_e32 v[42:43], v[10:11]
	v_mov_b64_e32 v[40:41], v[8:9]
	v_mov_b64_e32 v[38:39], v[6:7]
	v_mov_b64_e32 v[36:37], v[4:5]
	v_mov_b64_e32 v[34:35], v[2:3]
	v_mov_b64_e32 v[32:33], v[0:1]
	v_mov_b64_e32 v[28:29], v[12:13]
	v_mov_b64_e32 v[26:27], v[10:11]
	v_mov_b64_e32 v[24:25], v[8:9]
	v_mov_b64_e32 v[22:23], v[6:7]
	v_mov_b64_e32 v[20:21], v[4:5]
	v_mov_b64_e32 v[18:19], v[2:3]
	v_mov_b64_e32 v[16:17], v[0:1]
	v_mov_b64_e32 v[92:93], v[12:13]
	v_mov_b64_e32 v[90:91], v[10:11]
	v_mov_b64_e32 v[88:89], v[8:9]
	v_mov_b64_e32 v[86:87], v[6:7]
	v_mov_b64_e32 v[84:85], v[4:5]
	v_mov_b64_e32 v[82:83], v[2:3]
	v_mov_b64_e32 v[80:81], v[0:1]
	s_mov_b32 s35, 0
	s_waitcnt vmcnt(0)
	s_mul_hi_u32 s48, s15, 0xaaaaaaab
	s_lshr_b32 s48, s48, 1
	s_mul_i32 s48, s48, 0x18000
	s_sub_i32 s49, s60, s48
	s_sub_i32 s57, s61, s48
	s_add_i32 s49, s31, s49
	v_lshl_add_u64 v[2:3], v[150:151], 0, s[52:53]
	s_sub_i32 s58, s4, s48
	s_add_i32 m0, s90, s49
	v_lshl_add_u64 v[4:5], v[2:3], 0, s[36:37]
	s_add_i32 s49, s31, s57
	s_sub_i32 s48, s5, s48
	global_load_lds_dwordx4 v[4:5], off
	v_lshl_add_u64 v[4:5], v[148:149], 0, s[52:53]
	s_add_i32 m0, s90, s49
	s_add_i32 s49, s31, s58
	global_load_lds_dwordx4 v[4:5], off
	v_lshl_add_u64 v[2:3], v[2:3], 0, s[24:25]
	s_add_i32 m0, s90, s49
	s_add_i32 s48, s31, s48
	global_load_lds_dwordx4 v[2:3], off
	v_lshl_add_u64 v[2:3], v[146:147], 0, s[52:53]
	s_add_i32 m0, s90, s48
	s_nop 0
	global_load_lds_dwordx4 v[2:3], off
	v_lshl_add_u64 v[146:147], v[146:147], 0, s[68:69]
	v_lshl_add_u64 v[148:149], v[148:149], 0, s[68:69]
	v_lshl_add_u64 v[150:151], v[150:151], 0, s[68:69]
	ds_read_b128 v[2:5], v161
	ds_read_b128 v[6:9], v161 offset:8192
	ds_read_b128 v[10:13], v162
	ds_read_b128 v[166:169], v162 offset:8192
	ds_read_b128 v[186:189], v163
	ds_read_b128 v[190:193], v163 offset:8192
	ds_read_b128 v[218:221], v164
	ds_read_b128 v[222:225], v164 offset:8192
	s_cmp_le_i32 s28, s16
	s_cselect_b64 vcc, -1, 0
	s_waitcnt lgkmcnt(0)
	v_cndmask_b32_e32 v15, 0, v158, vcc
	v_sub_f32_e32 v96, v15, v165
	v_mov_b32_e32 v97, v96
	v_mov_b32_e32 v98, v96
	v_mov_b32_e32 v99, v96
	v_mov_b32_e32 v100, v96
	v_mov_b32_e32 v101, v96
	v_mov_b32_e32 v102, v96
	v_mov_b32_e32 v103, v96
	v_mov_b32_e32 v104, v96
	v_mov_b32_e32 v105, v96
	v_mov_b32_e32 v106, v96
	v_mov_b32_e32 v107, v96
	v_mov_b32_e32 v108, v96
	v_mov_b32_e32 v109, v96
	v_mov_b32_e32 v110, v96
	v_mov_b32_e32 v111, v96
	s_nop 1
	v_mfma_f32_32x32x16_bf16 v[112:127], v[2:5], v[128:131], v[96:111]
	v_mfma_f32_32x32x16_bf16 v[96:111], v[6:9], v[128:131], v[96:111]
	v_mfma_f32_32x32x16_bf16 v[112:127], v[10:13], v[132:135], v[112:127]
	v_mfma_f32_32x32x16_bf16 v[96:111], v[166:169], v[132:135], v[96:111]
	v_mfma_f32_32x32x16_bf16 v[112:127], v[186:189], v[136:139], v[112:127]
	v_mfma_f32_32x32x16_bf16 v[96:111], v[190:193], v[136:139], v[96:111]
	v_mfma_f32_32x32x16_bf16 v[112:127], v[218:221], v[140:143], v[112:127]
	v_mfma_f32_32x32x16_bf16 v[96:111], v[222:225], v[140:143], v[96:111]
	s_branch .LBB0_830

; #define LAS __attribute__((address_space(3)))
; #define MFMA32(a, b, c) __builtin_amdgcn_mfma_f32_32x32x16_bf16((a), (b), (c), 0, 0, 0)
;     __device__ __forceinline__ void init(const void* A_, const void* B_, int lda_, int ldb_, int M, unsigned mask_, int G_, int c_) { A = (const char*)A_; B = (const char*)B_; lda = lda_; ldb = ldb_; nM = M / BM; mask = mask_; nN = __builtin_popcount(mask_); nwg = nM * nN; G = G_; c = c_; }
;     __device__ __forceinline__ void init(f32x4 (&acc)[2][2][4][2], const Unit& u, int wr, int wc, int fr, int fq) const { u32x4 old[2][4][2]; init_load(old, u, wr, wc, fr, fq); init_finish(acc, old); }
; template <int KS> DI void at_qk(f32x16& p0, f32x16& p1, LAS const unsigned char* Kt, int mapB, const bf16x8 (&qr)[8], float init, int r32, int hi) {
; #pragma unroll
;     for (int i = 0; i < 16; ++i) { p0[i] = init; p1[i] = init; }
;     bf16x8 kb[KS][2];
; #pragma unroll
;     for (int d0 = 0; d0 < KS; ++d0) { const int cb = mapB + (d0 * 16 + hi * 8) * 2;
;         kb[d0][0] = *(const LAS bf16x8*)(Kt + AT_KSWZ(r32, cb)); kb[d0][1] = *(const LAS bf16x8*)(Kt + AT_KSWZ(32 + r32, cb)); }
;     __builtin_amdgcn_sched_barrier(0);
; #pragma unroll
;     for (int d0 = 0; d0 < KS; ++d0) { p0 = MFMA32(kb[d0][0], qr[d0], p0); p1 = MFMA32(kb[d0][1], qr[d0], p1); }
; DI float at_softmax(f32x16& p0, f32x16& p1, float& m_run, bool first, bool nearb, LAS const float* tabp, int lane) {
;     if (nearb) {
; #pragma unroll
;         for (int i = 0; i < 16; ++i) { p0[i] += tabp[8 * (i >> 2) + (i & 3)]; p1[i] += tabp[32 + 8 * (i >> 2) + (i & 3)]; }
;     }
;     float mx = p0[0];
; #pragma unroll
;     for (int i = 1; i < 16; ++i) mx = fmaxf(mx, p0[i]);
; #pragma unroll
;     for (int i = 0; i < 16; ++i) mx = fmaxf(mx, p1[i]);
.LBB0_837:
	v_add_u32_e32 v0, s100, v161
	ds_read_b128 v[2:5], v0
	ds_read_b128 v[6:9], v0 offset:8192
	v_add_u32_e32 v0, s100, v162
	ds_read_b128 v[10:13], v0
	ds_read_b128 v[166:169], v0 offset:8192
	v_add_u32_e32 v0, s100, v163
	ds_read_b128 v[186:189], v0
	ds_read_b128 v[190:193], v0 offset:8192
	v_add_u32_e32 v0, s100, v164
	ds_read_b128 v[218:221], v0
	ds_read_b128 v[222:225], v0 offset:8192
	s_add_i32 s101, s28, 64
	s_cmp_le_i32 s101, s16
	s_cselect_b64 vcc, -1, 0
	v_cndmask_b32_e32 v15, 0, v158, vcc
	v_sub_f32_e32 v232, v15, v165
	v_mov_b32_e32 v233, v232
	v_mov_b32_e32 v234, v232
	v_mov_b32_e32 v235, v232
	v_mov_b32_e32 v236, v232
	v_mov_b32_e32 v237, v232
	v_mov_b32_e32 v238, v232
	v_mov_b32_e32 v239, v232
	v_mov_b32_e32 v240, v232
	v_mov_b32_e32 v241, v232
	v_mov_b32_e32 v242, v232
	v_mov_b32_e32 v243, v232
	v_mov_b32_e32 v244, v232
	v_mov_b32_e32 v245, v232
	v_mov_b32_e32 v246, v232
	v_mov_b32_e32 v247, v232
	v_max_f32_e32 v0, v113, v113
	v_max_f32_e32 v14, v112, v112
	v_max_f32_e32 v0, v14, v0
	v_max3_f32 v0, v0, v114, v115
	v_max3_f32 v0, v0, v116, v117
	s_waitcnt lgkmcnt(0)
	v_mfma_f32_32x32x16_bf16 v[202:217], v[2:5], v[128:131], v[232:247]
	v_max3_f32 v0, v0, v118, v119
	v_max3_f32 v0, v0, v120, v121
	v_mfma_f32_32x32x16_bf16 v[232:247], v[6:9], v[128:131], v[232:247]
	v_max3_f32 v0, v0, v122, v123
	v_max3_f32 v0, v0, v124, v125
	v_mfma_f32_32x32x16_bf16 v[202:217], v[10:13], v[132:135], v[202:217]
	v_max3_f32 v0, v0, v126, v127
	v_max3_f32 v0, v0, v96, v97
	v_mfma_f32_32x32x16_bf16 v[232:247], v[166:169], v[132:135], v[232:247]
	v_max3_f32 v0, v0, v98, v99
	v_max3_f32 v0, v0, v100, v101
	v_mfma_f32_32x32x16_bf16 v[202:217], v[186:189], v[136:139], v[202:217]
	v_max3_f32 v0, v0, v102, v103
	v_max3_f32 v0, v0, v104, v105
	v_mfma_f32_32x32x16_bf16 v[232:247], v[190:193], v[136:139], v[232:247]
	v_max3_f32 v0, v0, v106, v107
	v_max3_f32 v0, v0, v108, v109
	s_xor_b64 s[58:59], s[42:43], -1
	v_max3_f32 v2, v0, v110, v111
	s_and_b64 vcc, exec, s[58:59]
	s_cbranch_vccz .LBB0_839
	s_mov_b32 s49, 0x41000000
	v_cmp_ge_f32_e32 vcc, s49, v2
	s_cmp_lg_u64 vcc, exec
	s_cselect_b64 s[58:59], -1, 0
	s_cbranch_execz .LBB0_840
	s_branch .LBB0_841

; #define MFMA32(a, b, c) __builtin_amdgcn_mfma_f32_32x32x16_bf16((a), (b), (c), 0, 0, 0)
; template <int OFF> DI s16x4 at_tr_read(int vb) { s16x4 r; asm volatile("ds_read_b64_tr_b16 %0, %1 offset:%2" : "=&v"(r) : "v"(vb), "i"(OFF) : "memory"); return r; }
; DI unsigned at_cvtpk(float lo, float hi) { unsigned r; asm volatile("v_cvt_pk_bf16_f32 %0, %1, %2" : "=v"(r) : "v"(lo), "v"(hi)); return r; }
; DI float at_softmax(f32x16& p0, f32x16& p1, float& m_run, bool first, bool nearb, LAS const float* tabp, int lane) {
;     ...
;     for (int i = 0; i < 16; ++i) p0[i] = __builtin_amdgcn_exp2f(p0[i]);
; #pragma unroll
;     for (int i = 0; i < 16; ++i) p1[i] = __builtin_amdgcn_exp2f(p1[i]);
;     return alpha;
; }
; DI bf16x8 at_pack(const f32x16& p, int s8) {
;     u32x4 w; w.x = at_cvtpk(p[s8], p[s8 + 1]); w.y = at_cvtpk(p[s8 + 2], p[s8 + 3]); w.z = at_cvtpk(p[s8 + 4], p[s8 + 5]); w.w = at_cvtpk(p[s8 + 6], p[s8 + 7]);
;     return __builtin_bit_cast(bf16x8, w);
; }
; template <int D0> DI void at_pv_block(f32x16 (&o)[4], int vb, const bf16x8 (&pf)[4]) {
;     const s16x4 l0 = at_tr_read<D0 * 512 + 0 * 4096>(vb), h0 = at_tr_read<D0 * 512 + 0 * 4096 + 2048>(vb), l1 = at_tr_read<D0 * 512 + 1 * 4096>(vb), h1 = at_tr_read<D0 * 512 + 1 * 4096 + 2048>(vb);
;     const s16x4 l2 = at_tr_read<D0 * 512 + 2 * 4096>(vb), h2 = at_tr_read<D0 * 512 + 2 * 4096 + 2048>(vb), l3 = at_tr_read<D0 * 512 + 3 * 4096>(vb), h3 = at_tr_read<D0 * 512 + 3 * 4096 + 2048>(vb);
;     asm volatile("s_waitcnt lgkmcnt(0)" ::: "memory"); __builtin_amdgcn_sched_barrier(0);
;     ...
;     o[D0] = MFMA32(AT_PK(l0, h0), pf[0], o[D0]); o[D0] = MFMA32(AT_PK(l1, h1), pf[1], o[D0]); o[D0] = MFMA32(AT_PK(l2, h2), pf[2], o[D0]); o[D0] = MFMA32(AT_PK(l3, h3), pf[3], o[D0]);
; DI void attn_unit_diff(const Ctx& C, int l, int b, int h, int j) {
;     ...
;             pf[0] = at_pack(p0, 0); pf[1] = at_pack(p0, 8); pf[2] = at_pack(p1, 0); pf[3] = at_pack(p1, 8);
;             ol = MFMA32(ones, pf[0], ol); ol = MFMA32(ones, pf[1], ol); ol = MFMA32(ones, pf[2], ol); ol = MFMA32(ones, pf[3], ol);
;             at_pv_block<0>(o, vb, pf); at_pv_block<1>(o, vb, pf); at_pv_block<2>(o, vb, pf); at_pv_block<3>(o, vb, pf);
.LBB0_844:
	v_subrev_u32_e32 v87, s48, v160
	v_add_u32_e32 v87, s31, v87
	ds_read_b64_tr_b16 v[170:171], v87 offset:0x0
	ds_read_b64_tr_b16 v[172:173], v87 offset:0x800
	ds_read_b64_tr_b16 v[174:175], v87 offset:0x200
	ds_read_b64_tr_b16 v[176:177], v87 offset:0xa00
	ds_read_b64_tr_b16 v[178:179], v87 offset:0x400
	ds_read_b64_tr_b16 v[180:181], v87 offset:0xc00
	ds_read_b64_tr_b16 v[182:183], v87 offset:0x600
	ds_read_b64_tr_b16 v[184:185], v87 offset:0xe00
	v_exp_f32_e32 v112, v112
	v_exp_f32_e32 v113, v113
	v_mfma_f32_32x32x16_bf16 v[202:217], v[218:221], v[140:143], v[202:217]
	v_exp_f32_e32 v114, v114
	v_exp_f32_e32 v115, v115
	v_mfma_f32_32x32x16_bf16 v[232:247], v[222:225], v[140:143], v[232:247]
	v_exp_f32_e32 v116, v116
	v_exp_f32_e32 v117, v117
	v_exp_f32_e32 v118, v118
	v_exp_f32_e32 v119, v119
	v_cvt_pk_bf16_f32 v2, v112, v113
	v_cvt_pk_bf16_f32 v3, v114, v115
	v_cvt_pk_bf16_f32 v4, v116, v117
	v_cvt_pk_bf16_f32 v5, v118, v119
	v_add_f32_e32 v81, v112, v113
	v_add_f32_e32 v82, v114, v115
	v_add_f32_e32 v83, v116, v117
	v_add_f32_e32 v84, v118, v119
	v_add_f32_e32 v81, v81, v82
	v_add_f32_e32 v83, v83, v84
	v_add_f32_e32 v81, v81, v83
	v_add_f32_e32 v80, v80, v81
	s_waitcnt lgkmcnt(0)
	ds_read_b64_tr_b16 v[112:113], v87 offset:0x1000
	ds_read_b64_tr_b16 v[114:115], v87 offset:0x1800
	ds_read_b64_tr_b16 v[116:117], v87 offset:0x1200
	ds_read_b64_tr_b16 v[118:119], v87 offset:0x1a00
	ds_read_b64_tr_b16 v[88:89], v87 offset:0x1400
	ds_read_b64_tr_b16 v[90:91], v87 offset:0x1c00
	ds_read_b64_tr_b16 v[92:93], v87 offset:0x1600
	ds_read_b64_tr_b16 v[94:95], v87 offset:0x1e00
	v_mfma_f32_32x32x16_bf16 v[64:79], v[170:173], v[2:5], v[64:79]
	v_exp_f32_e32 v120, v120
	v_exp_f32_e32 v121, v121
	v_mfma_f32_32x32x16_bf16 v[48:63], v[174:177], v[2:5], v[48:63]
	v_exp_f32_e32 v122, v122
	v_exp_f32_e32 v123, v123
	v_mfma_f32_32x32x16_bf16 v[32:47], v[178:181], v[2:5], v[32:47]
	v_exp_f32_e32 v124, v124
	v_exp_f32_e32 v125, v125
	v_mfma_f32_32x32x16_bf16 v[16:31], v[182:185], v[2:5], v[16:31]
	v_exp_f32_e32 v126, v126
	v_exp_f32_e32 v127, v127
	v_cvt_pk_bf16_f32 v6, v120, v121
	v_cvt_pk_bf16_f32 v7, v122, v123
	v_cvt_pk_bf16_f32 v8, v124, v125
	v_cvt_pk_bf16_f32 v9, v126, v127
	v_add_f32_e32 v81, v120, v121
	v_add_f32_e32 v82, v122, v123
	v_add_f32_e32 v83, v124, v125
	v_add_f32_e32 v84, v126, v127
	v_add_f32_e32 v81, v81, v82
	v_add_f32_e32 v83, v83, v84
	v_add_f32_e32 v81, v81, v83
	v_add_f32_e32 v80, v80, v81
	s_waitcnt lgkmcnt(0)
	ds_read_b64_tr_b16 v[170:171], v87 offset:0x2000
	ds_read_b64_tr_b16 v[172:173], v87 offset:0x2800
	ds_read_b64_tr_b16 v[174:175], v87 offset:0x2200
	ds_read_b64_tr_b16 v[176:177], v87 offset:0x2a00
	ds_read_b64_tr_b16 v[178:179], v87 offset:0x2400
	ds_read_b64_tr_b16 v[180:181], v87 offset:0x2c00
	ds_read_b64_tr_b16 v[182:183], v87 offset:0x2600
	ds_read_b64_tr_b16 v[184:185], v87 offset:0x2e00
	v_mfma_f32_32x32x16_bf16 v[64:79], v[112:115], v[6:9], v[64:79]
	v_exp_f32_e32 v96, v96
	v_exp_f32_e32 v97, v97
	v_mfma_f32_32x32x16_bf16 v[48:63], v[116:119], v[6:9], v[48:63]
	v_exp_f32_e32 v98, v98
	v_exp_f32_e32 v99, v99
	v_mfma_f32_32x32x16_bf16 v[32:47], v[88:91], v[6:9], v[32:47]
	v_exp_f32_e32 v100, v100
	v_exp_f32_e32 v101, v101
	v_mfma_f32_32x32x16_bf16 v[16:31], v[92:95], v[6:9], v[16:31]
	v_exp_f32_e32 v102, v102
	v_exp_f32_e32 v103, v103
	v_cvt_pk_bf16_f32 v10, v96, v97
	v_cvt_pk_bf16_f32 v11, v98, v99
	v_cvt_pk_bf16_f32 v12, v100, v101
	v_cvt_pk_bf16_f32 v13, v102, v103
	v_add_f32_e32 v81, v96, v97
	v_add_f32_e32 v82, v98, v99
	v_add_f32_e32 v83, v100, v101
	v_add_f32_e32 v84, v102, v103
	v_add_f32_e32 v81, v81, v82
	v_add_f32_e32 v83, v83, v84
	v_add_f32_e32 v81, v81, v83
	v_add_f32_e32 v80, v80, v81
	s_waitcnt lgkmcnt(0)
	ds_read_b64_tr_b16 v[112:113], v87 offset:0x3000
	ds_read_b64_tr_b16 v[114:115], v87 offset:0x3800
	ds_read_b64_tr_b16 v[116:117], v87 offset:0x3200
	ds_read_b64_tr_b16 v[118:119], v87 offset:0x3a00
	ds_read_b64_tr_b16 v[88:89], v87 offset:0x3400
	ds_read_b64_tr_b16 v[90:91], v87 offset:0x3c00
	ds_read_b64_tr_b16 v[92:93], v87 offset:0x3600
	ds_read_b64_tr_b16 v[94:95], v87 offset:0x3e00
	v_mfma_f32_32x32x16_bf16 v[64:79], v[170:173], v[10:13], v[64:79]
	v_exp_f32_e32 v104, v104
	v_exp_f32_e32 v105, v105
	v_mfma_f32_32x32x16_bf16 v[48:63], v[174:177], v[10:13], v[48:63]
	v_exp_f32_e32 v106, v106
	v_exp_f32_e32 v107, v107
	v_mfma_f32_32x32x16_bf16 v[32:47], v[178:181], v[10:13], v[32:47]
	v_exp_f32_e32 v108, v108
	v_exp_f32_e32 v109, v109
	v_mfma_f32_32x32x16_bf16 v[16:31], v[182:185], v[10:13], v[16:31]
	v_exp_f32_e32 v110, v110
	v_exp_f32_e32 v111, v111
	v_cvt_pk_bf16_f32 v166, v104, v105
	v_cvt_pk_bf16_f32 v167, v106, v107
	v_cvt_pk_bf16_f32 v168, v108, v109
	v_cvt_pk_bf16_f32 v169, v110, v111
	v_add_f32_e32 v81, v104, v105
	v_add_f32_e32 v82, v106, v107
	v_add_f32_e32 v83, v108, v109
	v_add_f32_e32 v84, v110, v111
	v_add_f32_e32 v81, v81, v82
	v_add_f32_e32 v83, v83, v84
	v_add_f32_e32 v81, v81, v83
	v_add_f32_e32 v80, v80, v81
	s_waitcnt lgkmcnt(0)
	v_mfma_f32_32x32x16_bf16 v[64:79], v[112:115], v[166:169], v[64:79]
	v_mov_b64_e32 v[96:97], v[232:233]
	v_mov_b64_e32 v[98:99], v[234:235]
	v_mov_b64_e32 v[100:101], v[236:237]
	v_mov_b64_e32 v[102:103], v[238:239]
	v_mfma_f32_32x32x16_bf16 v[48:63], v[116:119], v[166:169], v[48:63]
	v_mov_b64_e32 v[104:105], v[240:241]
	v_mov_b64_e32 v[106:107], v[242:243]
	v_mov_b64_e32 v[108:109], v[244:245]
	v_mov_b64_e32 v[110:111], v[246:247]
	v_mfma_f32_32x32x16_bf16 v[32:47], v[88:91], v[166:169], v[32:47]
	v_mov_b64_e32 v[120:121], v[210:211]
	v_mov_b64_e32 v[122:123], v[212:213]
	v_mov_b64_e32 v[124:125], v[214:215]
	v_mov_b64_e32 v[126:127], v[216:217]
	v_mfma_f32_32x32x16_bf16 v[16:31], v[92:95], v[166:169], v[16:31]
	v_mov_b64_e32 v[112:113], v[202:203]
	v_mov_b64_e32 v[114:115], v[204:205]
	v_mov_b64_e32 v[116:117], v[206:207]
	v_mov_b64_e32 v[118:119], v[208:209]
	s_mov_b64 s[42:43], 0
	s_mov_b64 s[58:59], -1
	s_and_b64 vcc, exec, s[76:77]
	s_cbranch_vccz .LBB0_833

; DI float max_x32(float v, int lane) { return fmaxf(v, bpx(v, lane, 32)); }
; DI float at_softmax(f32x16& p0, f32x16& p1, float& m_run, bool first, bool nearb, LAS const float* tabp, int lane) {
;     ...
;     if (first || !__all(mx <= AT_THR)) {
;         mx = max_x32(mx, lane);
;         const float dl = first ? mx : fmaxf(mx, 0.f);
;         alpha = first ? 1.f : __builtin_amdgcn_exp2f(-dl); m_run += dl;
; #pragma unroll
;         for (int i = 0; i < 16; ++i) { p0[i] -= dl; p1[i] -= dl; }
;     }
.LBB0_847:
	ds_bpermute_b32 v0, v157, v2
	v_max_f32_e32 v2, v2, v2
	s_waitcnt lgkmcnt(0)
	v_max_f32_e32 v0, v0, v0
	v_max_f32_e32 v0, v2, v0
	v_max_f32_e32 v2, 0, v0
	v_cndmask_b32_e64 v0, v2, v0, s[42:43]
	v_exp_f32_e64 v2, -v0
	v_add_f32_e32 v165, v165, v0
	v_pk_add_f32 v[112:113], v[112:113], v[0:1] op_sel_hi:[1,0] neg_lo:[0,1] neg_hi:[0,1]
	v_pk_add_f32 v[96:97], v[96:97], v[0:1] op_sel_hi:[1,0] neg_lo:[0,1] neg_hi:[0,1]
	v_pk_add_f32 v[114:115], v[114:115], v[0:1] op_sel_hi:[1,0] neg_lo:[0,1] neg_hi:[0,1]
	v_pk_add_f32 v[98:99], v[98:99], v[0:1] op_sel_hi:[1,0] neg_lo:[0,1] neg_hi:[0,1]
	v_pk_add_f32 v[116:117], v[116:117], v[0:1] op_sel_hi:[1,0] neg_lo:[0,1] neg_hi:[0,1]
	v_pk_add_f32 v[100:101], v[100:101], v[0:1] op_sel_hi:[1,0] neg_lo:[0,1] neg_hi:[0,1]
	v_pk_add_f32 v[118:119], v[118:119], v[0:1] op_sel_hi:[1,0] neg_lo:[0,1] neg_hi:[0,1]
	v_pk_add_f32 v[102:103], v[102:103], v[0:1] op_sel_hi:[1,0] neg_lo:[0,1] neg_hi:[0,1]
	v_pk_add_f32 v[120:121], v[120:121], v[0:1] op_sel_hi:[1,0] neg_lo:[0,1] neg_hi:[0,1]
	v_pk_add_f32 v[104:105], v[104:105], v[0:1] op_sel_hi:[1,0] neg_lo:[0,1] neg_hi:[0,1]
	v_pk_add_f32 v[122:123], v[122:123], v[0:1] op_sel_hi:[1,0] neg_lo:[0,1] neg_hi:[0,1]
	v_pk_add_f32 v[106:107], v[106:107], v[0:1] op_sel_hi:[1,0] neg_lo:[0,1] neg_hi:[0,1]
	v_pk_add_f32 v[124:125], v[124:125], v[0:1] op_sel_hi:[1,0] neg_lo:[0,1] neg_hi:[0,1]
	v_pk_add_f32 v[108:109], v[108:109], v[0:1] op_sel_hi:[1,0] neg_lo:[0,1] neg_hi:[0,1]
	v_pk_add_f32 v[126:127], v[126:127], v[0:1] op_sel_hi:[1,0] neg_lo:[0,1] neg_hi:[0,1]
	v_pk_add_f32 v[110:111], v[110:111], v[0:1] op_sel_hi:[1,0] neg_lo:[0,1] neg_hi:[0,1]
	s_nop 15
	v_pk_add_f32 v[202:203], v[202:203], v[0:1] op_sel_hi:[1,0] neg_lo:[0,1] neg_hi:[0,1]
	v_pk_add_f32 v[204:205], v[204:205], v[0:1] op_sel_hi:[1,0] neg_lo:[0,1] neg_hi:[0,1]
	v_pk_add_f32 v[206:207], v[206:207], v[0:1] op_sel_hi:[1,0] neg_lo:[0,1] neg_hi:[0,1]
	v_pk_add_f32 v[208:209], v[208:209], v[0:1] op_sel_hi:[1,0] neg_lo:[0,1] neg_hi:[0,1]
	v_pk_add_f32 v[210:211], v[210:211], v[0:1] op_sel_hi:[1,0] neg_lo:[0,1] neg_hi:[0,1]
	v_pk_add_f32 v[212:213], v[212:213], v[0:1] op_sel_hi:[1,0] neg_lo:[0,1] neg_hi:[0,1]
	v_pk_add_f32 v[214:215], v[214:215], v[0:1] op_sel_hi:[1,0] neg_lo:[0,1] neg_hi:[0,1]
	v_pk_add_f32 v[216:217], v[216:217], v[0:1] op_sel_hi:[1,0] neg_lo:[0,1] neg_hi:[0,1]
	v_pk_add_f32 v[232:233], v[232:233], v[0:1] op_sel_hi:[1,0] neg_lo:[0,1] neg_hi:[0,1]
	v_pk_add_f32 v[234:235], v[234:235], v[0:1] op_sel_hi:[1,0] neg_lo:[0,1] neg_hi:[0,1]
	v_pk_add_f32 v[236:237], v[236:237], v[0:1] op_sel_hi:[1,0] neg_lo:[0,1] neg_hi:[0,1]
	v_pk_add_f32 v[238:239], v[238:239], v[0:1] op_sel_hi:[1,0] neg_lo:[0,1] neg_hi:[0,1]
	v_pk_add_f32 v[240:241], v[240:241], v[0:1] op_sel_hi:[1,0] neg_lo:[0,1] neg_hi:[0,1]
	v_pk_add_f32 v[242:243], v[242:243], v[0:1] op_sel_hi:[1,0] neg_lo:[0,1] neg_hi:[0,1]
	v_pk_add_f32 v[244:245], v[244:245], v[0:1] op_sel_hi:[1,0] neg_lo:[0,1] neg_hi:[0,1]
	v_pk_add_f32 v[246:247], v[246:247], v[0:1] op_sel_hi:[1,0] neg_lo:[0,1] neg_hi:[0,1]
	v_cndmask_b32_e64 v0, v2, 1.0, s[42:43]
	v_cmp_neq_f32_e32 vcc, 1.0, v0
	s_cbranch_vccnz .LBB0_843
	s_branch .LBB0_844
